# baseline (speedup 1.0000x reference)
.Lk2_epi:
	s_waitcnt vmcnt(0) lgkmcnt(0)
	s_nop 15
	s_barrier
	v_lshlrev_b32_e32 v180, 12, v171
	v_lshlrev_b32_e32 v181, 6, v172
	v_lshlrev_b32_e32 v182, 3, v173
	v_or3_b32 v181, v180, v181, v182
	v_add_u32_e32 v182, 0x800, v181
	v_cvt_pk_f16_f32 v184, v16, v17
	v_cvt_pk_f16_f32 v185, v18, v19
	v_cvt_pk_f16_f32 v186, v20, v21
	v_cvt_pk_f16_f32 v187, v22, v23
	v_cvt_pk_f16_f32 v188, v24, v25
	v_cvt_pk_f16_f32 v189, v26, v27
	v_cvt_pk_f16_f32 v190, v28, v29
	v_cvt_pk_f16_f32 v191, v30, v31
	ds_write2_b64 v181, v[184:185], v[186:187] offset1:2
	ds_write2_b64 v181, v[188:189], v[190:191] offset0:4 offset1:6
	v_cvt_pk_f16_f32 v184, v0, v1
	v_cvt_pk_f16_f32 v185, v2, v3
	v_cvt_pk_f16_f32 v186, v4, v5
	v_cvt_pk_f16_f32 v187, v6, v7
	v_cvt_pk_f16_f32 v188, v8, v9
	v_cvt_pk_f16_f32 v189, v10, v11
	v_cvt_pk_f16_f32 v190, v12, v13
	v_cvt_pk_f16_f32 v191, v14, v15
	ds_write2_b64 v182, v[184:185], v[186:187] offset1:2
	ds_write2_b64 v182, v[188:189], v[190:191] offset0:4 offset1:6
	s_lshl_b32 s36, s10, 18
	s_add_u32 s0, s6, s36
	s_addc_u32 s1, s7, 0
	s_lshl_b32 s36, s11, 3
	s_add_u32 s36, s36, s33
	s_lshl_b32 s36, s36, 12
	s_add_u32 s0, s0, s36
	s_addc_u32 s1, s1, 0
	v_or_b32_e32 v183, v180, v160
	s_waitcnt lgkmcnt(0)
	ds_read_b128 v[0:3], v183
	ds_read_b128 v[4:7], v183 offset:1024
	ds_read_b128 v[8:11], v183 offset:2048
	ds_read_b128 v[12:15], v183 offset:3072
	s_waitcnt lgkmcnt(3)
	global_store_dwordx4 v160, v[0:3], s[0:1] nt
	s_waitcnt lgkmcnt(2)
	global_store_dwordx4 v160, v[4:7], s[0:1] offset:1024 nt
	s_waitcnt lgkmcnt(1)
	global_store_dwordx4 v160, v[8:11], s[0:1] offset:2048 nt
	s_waitcnt lgkmcnt(0)
	global_store_dwordx4 v160, v[12:15], s[0:1] offset:3072 nt
	s_endpgm
